# v19 + attention queue: next unit index fetched one unit ahead (atomic issued at unit start, published after the bias-table barrier), no barriers at unit start
# baseline (speedup 1.0000x reference)
.LBB0_650:
	s_lshl_b32 s2, s2, 3
	s_ashr_i32 s3, s2, 31
	v_readlane_b32 s12, v253, 20
	s_xor_b32 s3, s3, s12
	s_abs_i32 s2, s2
	v_readlane_b32 s12, v254, 33
	s_mul_hi_u32 s12, s2, s12
	v_readlane_b32 s17, v254, 32
	s_mul_i32 s13, s12, s17
	s_sub_i32 s2, s2, s13
	s_add_i32 s13, s12, 1
	s_sub_i32 s16, s2, s17
	s_cmp_ge_u32 s2, s17
	s_cselect_b32 s12, s13, s12
	s_cselect_b32 s2, s16, s2
	s_add_i32 s13, s12, 1
	s_cmp_ge_u32 s2, s17
	s_cselect_b32 s2, s13, s12
	s_xor_b32 s2, s2, s3
	s_sub_i32 s2, s2, s3
	s_and_b32 s12, s2, 7
	v_readlane_b32 s2, v253, 32
	v_readlane_b32 s3, v253, 33
	s_lshl_b32 s2, s2, 8
	s_lshl_b32 s3, s12, 5
	s_or_b32 s96, s3, s2
	s_lshl_b64 s[2:3], s[96:97], 2
	v_readlane_b32 s13, v254, 22
	s_add_u32 s52, s13, s2
	v_readlane_b32 s2, v254, 23
	s_addc_u32 s53, s2, s3
	s_mul_i32 s2, s12, 0x2800000
	s_add_u32 s78, s24, s2
	s_addc_u32 s79, s25, 0
	s_add_u32 s28, s78, 0x4d000000
	s_addc_u32 s29, s79, 0
	s_add_u32 s54, s78, 0x4d000400
	s_addc_u32 s55, s79, 0
	s_add_u32 s56, s78, 0x4d000800
	s_addc_u32 s57, s79, 0
	s_add_u32 s2, s14, s2
	s_addc_u32 s3, s15, 0
	s_add_u32 s58, s2, 0x91000000
	s_addc_u32 s59, s3, 0
	s_lshl_b32 s2, s12, 17
	s_add_u32 s0, s0, s2
	s_addc_u32 s1, s1, 0
	s_add_u32 s60, s0, 0x6d900000
	s_addc_u32 s61, s1, 0
	s_and_saveexec_b64 s[14:15], s[90:91]
	s_cbranch_execz .Lattq_first
	v_mov_b32_e32 v127, 1
	global_atomic_add v127, v187, v127, s[52:53] sc0
	s_waitcnt vmcnt(0)
	ds_write_b32 v187, v127 offset:240
.Lattq_first:
	s_mov_b64 exec, s[14:15]
	s_waitcnt lgkmcnt(0)
	s_barrier
	s_branch .LBB0_653

.LBB0_653:
	ds_read_b32 v1, v187 offset:240
	s_mov_b64 s[0:1], -1
	s_waitcnt lgkmcnt(0)
	v_readfirstlane_b32 s2, v1
	s_cmpk_gt_i32 s2, 0x7f
	s_cbranch_scc1 .LBB0_652
	s_and_saveexec_b64 s[14:15], s[90:91]
	s_cbranch_execz .Lattq_nopf
	v_mov_b32_e32 v127, 1
	global_atomic_add v127, v187, v127, s[52:53] sc0
.Lattq_nopf:
	s_mov_b64 exec, s[14:15]
	s_lshl_b32 s0, s2, 5
	s_and_b32 s12, s0, 0xffffff00
	s_andn2_b32 s33, 7, s2
	s_sub_i32 s0, 0xf00, s12
	s_ashr_i32 s1, s0, 31
	s_lshl_b32 s2, s33, 14
	s_add_u32 s14, s60, s2
	s_addc_u32 s15, s61, 0
	s_lshl_b64 s[2:3], s[0:1], 2
	s_add_u32 s2, s14, s2
	s_addc_u32 s3, s15, s3
	v_mov_b32_e32 v66, v0
	v_mov_b64_e32 v[2:3], s[2:3]
	global_load_dword v1, v[2:3], off
	s_sub_i32 s68, 0x1000, s12
	v_readfirstlane_b32 s2, v66
	v_cmp_gt_i32_e32 vcc, s68, v66
	v_mov_b32_e32 v14, 0
	v_ashrrev_i32_e32 v67, 31, v66
	v_mov_b32_e32 v15, 0
	s_and_saveexec_b64 s[24:25], vcc
	s_cbranch_execz .LBB0_660
	v_lshl_add_u64 v[2:3], v[66:67], 2, s[14:15]
	global_load_dword v15, v[2:3], off

.LBB0_682:
	s_or_b64 exec, exec, s[14:15]
	s_waitcnt lgkmcnt(0)
	s_barrier
	s_waitcnt vmcnt(0) lgkmcnt(0)
	s_and_saveexec_b64 s[14:15], s[90:91]
	s_cbranch_execz .Lattq_nowr
	ds_write_b32 v187, v127 offset:240
.Lattq_nowr:
	s_mov_b64 exec, s[14:15]
	v_and_b32_e32 v1, 63, v66
	s_ashr_i32 s46, s68, 6
	v_cmp_gt_i32_e32 vcc, s46, v1
	s_mov_b64 s[14:15], 0
	s_and_saveexec_b64 s[24:25], vcc
	s_cbranch_execz .LBB0_684
	s_add_i32 s3, 0, 0x15800
	v_lshl_add_u32 v2, v1, 8, s3
	ds_read_b32 v2, v2 offset:252
	s_mov_b32 s3, 0xc2800000
	s_waitcnt lgkmcnt(0)
	v_cmp_gt_f32_e32 vcc, s3, v2
	s_and_b64 s[14:15], vcc, exec
